# baseline (speedup 1.0000x reference)
.LBB1_5:
	s_waitcnt lgkmcnt(6)
	v_mfma_f32_32x32x64_f8f6f4 v[4:19], v[156:163], v[148:155], v[4:19]
	v_cmp_eq_u32_e32 vcc, 0, v1
	s_nop 1
	s_and_saveexec_b64 s[0:1], vcc
	s_lshl_b32 s12, s29, 2
	s_add_i32 s12, s12, 0x12000
	v_mov_b32_e32 v1, s12
	ds_write_b32 v1, v0
	s_or_b64 exec, exec, s[0:1]
	s_waitcnt vmcnt(0) lgkmcnt(0)
	s_barrier
	v_mov_b32_e32 v104, 0
	v_mov_b32_e32 v206, 0x12000
	ds_read_b128 v[38:41], v206
	ds_read_b128 v[42:45], v206 offset:16
	s_mov_b32 s14, 0
	v_mfma_f32_32x32x64_f8f6f4 v[20:35], v[164:171], v[148:155], v[20:35]
	v_mfma_f32_32x32x64_f8f6f4 v[4:19], v[80:87], v[72:79], v[4:19]
	v_mfma_f32_32x32x64_f8f6f4 v[20:35], v[58:65], v[72:79], v[20:35]
	s_waitcnt lgkmcnt(0)
	v_or_b32_e32 v0, v39, v38
	v_or_b32_e32 v0, v40, v0
	v_or_b32_e32 v0, v41, v0
	v_or_b32_e32 v0, v42, v0
	v_or_b32_e32 v0, v43, v0
	v_or_b32_e32 v0, v44, v0
	v_or_b32_e32 v0, v45, v0
	v_cmp_ne_u32_e32 vcc, 0, v0
	s_cbranch_vccnz .LBB1_13
	s_mov_b64 s[0:1], -1
	s_nop 7
	v_mov_b64_e32 v[54:55], v[4:5]
	v_mov_b64_e32 v[56:57], v[6:7]
	v_mov_b64_e32 v[58:59], v[8:9]
	v_mov_b64_e32 v[60:61], v[10:11]
	v_mov_b64_e32 v[62:63], v[12:13]
	v_mov_b64_e32 v[64:65], v[14:15]
	v_mov_b64_e32 v[66:67], v[16:17]
	v_mov_b64_e32 v[68:69], v[18:19]
	v_mov_b64_e32 v[38:39], v[20:21]
	v_mov_b64_e32 v[40:41], v[22:23]
	v_mov_b64_e32 v[42:43], v[24:25]
	v_mov_b64_e32 v[44:45], v[26:27]
	v_mov_b64_e32 v[46:47], v[28:29]
	v_mov_b64_e32 v[48:49], v[30:31]
	v_mov_b64_e32 v[50:51], v[32:33]
	v_mov_b64_e32 v[52:53], v[34:35]
	s_branch .Lfinal_copy
